# v39 + P3 prologue: bias-table and k/q-norm gain loads issued together before one wait (were three dependent rounds)
# speedup vs baseline: 1.0036x; 1.0036x over previous
.LBB0_695:
	s_add_i32 s2, 0, 0x27e10
	v_mov_b32_e32 v46, s2
	ds_read_b64 v[46:47], v46
	s_add_i32 s2, 0, 0x27e38
	v_mov_b32_e32 v84, s2
	ds_read_b64 v[84:85], v84
	s_add_i32 s2, 0, 0x27e40
	v_mov_b32_e32 v86, s2
	ds_read_b64 v[86:87], v86
	s_waitcnt lgkmcnt(0)
	v_readfirstlane_b32 s4, v46
	v_readfirstlane_b32 s5, v47
	v_readfirstlane_b32 s6, v84
	v_readfirstlane_b32 s7, v85
	v_readfirstlane_b32 s8, v86
	v_readfirstlane_b32 s9, v87
	v_lshlrev_b32_e32 v46, 2, v0
	s_nop 4
	global_load_dword v84, v46, s[4:5]
	s_cmp_gt_u32 s88, 3
	s_cbranch_scc1 .Lp3pro_w
	global_load_dword v85, v46, s[4:5] offset:2048
	s_cmp_gt_u32 s88, 1
	s_cbranch_scc1 .Lp3pro_q
	global_load_dword v86, v46, s[8:9]
	s_branch .Lp3pro_w
.Lp3pro_q:
	global_load_dword v86, v46, s[6:7] offset:-512
.Lp3pro_w:
	v_add_u32_e32 v47, 0x22400, v46
	s_waitcnt vmcnt(0)
	ds_write_b32 v47, v84
	s_cmp_gt_u32 s88, 3
	s_cbranch_scc1 .LBB0_704
	ds_write_b32 v47, v85 offset:2048
	v_add_u32_e32 v47, 0x23000, v46
	ds_write_b32 v47, v86
.LBB0_704:
	v_lshrrev_b32_e32 v141, 4, v196
	s_andn2_b64 vcc, exec, s[0:1]
	v_lshrrev_b32_e32 v142, 2, v140
	s_waitcnt lgkmcnt(0)
	s_barrier
	s_cbranch_vccnz .LBB0_810
	v_lshlrev_b32_e32 v46, 3, v0
	v_and_b32_e32 v143, 0x78, v46
	v_mbcnt_lo_u32_b32 v46, -1, 0
	v_mbcnt_hi_u32_b32 v47, -1, v46
	v_and_b32_e32 v84, 64, v47
	v_xor_b32_e32 v46, 1, v47
	v_add_u32_e32 v85, 64, v84
	v_cmp_lt_i32_e32 vcc, v46, v85
	s_add_i32 s0, 0, 0x23000
	s_lshl_b32 s3, s88, 4
	v_cndmask_b32_e32 v46, v47, v46, vcc
	v_lshlrev_b32_e32 v145, 2, v46
	v_xor_b32_e32 v46, 2, v47
	v_writelane_b32 v254, s86, 13
	v_lshl_add_u32 v144, v143, 2, s0
	v_cmp_lt_i32_e32 vcc, v46, v85
	s_mov_b32 s0, s88
	s_and_b32 s33, s3, 0x3fffffe0
	v_lshlrev_b32_e32 v136, 2, v141
	v_cndmask_b32_e32 v46, v47, v46, vcc
	v_writelane_b32 v254, s0, 14
	v_and_b32_e32 v86, 48, v0
	v_or_b32_e32 v92, s33, v136
	v_lshlrev_b32_e32 v93, 2, v0
	v_lshlrev_b32_e32 v146, 2, v46
	v_xor_b32_e32 v46, 4, v47
	v_writelane_b32 v254, s1, 15
	v_add_u32_e32 v90, 0, v86
	v_or_b32_e32 v87, v92, v142
	v_and_b32_e32 v86, 12, v93
	s_movk_i32 s0, 0x88
	v_cmp_lt_i32_e32 vcc, v46, v85
	s_add_i32 s2, 0, 0x11000
	v_mad_u64_u32 v[86:87], s[0:1], v87, s0, v[86:87]
	v_cndmask_b32_e32 v46, v47, v46, vcc
	v_lshl_add_u32 v150, v86, 1, s2
	v_mul_u32_u24_e32 v86, 0x88, v1
	v_lshlrev_b32_e32 v147, 2, v46
	v_xor_b32_e32 v46, 8, v47
	v_lshlrev_b32_e32 v88, 1, v143
	v_or_b32_e32 v149, s3, v140
	v_lshlrev_b32_e32 v86, 1, v86
	v_cmp_lt_i32_e32 vcc, v46, v85
	v_add_u32_e32 v91, 0x80, v149
	v_cmp_gt_u32_e64 s[0:1], 16, v196
	v_add3_u32 v151, 0, v88, v86
	v_add3_u32 v152, s2, v88, v86
	v_xor_b32_e32 v86, 16, v47
	v_cndmask_b32_e32 v46, v47, v46, vcc
	v_writelane_b32 v254, s0, 16
	v_cmp_lt_i32_e32 vcc, v86, v85
	v_sub_u32_e32 v99, v91, v92
	s_movk_i32 s8, 0x81
	v_writelane_b32 v254, s1, 17
	v_cndmask_b32_e32 v86, v47, v86, vcc
	s_or_b32 s2, s3, 16
	s_add_i32 s3, s33, 32
	s_add_i32 s4, s33, 48
	s_add_i32 s5, s33, 64
	s_add_i32 s6, s33, 0x50
	s_add_i32 s7, s33, 0x60
	s_add_i32 s9, s33, 0x70
	s_add_i32 s11, s33, 0x80
	s_add_i32 s0, s33, 0x90
	v_cmp_gt_u32_e64 s[12:13], s8, v99
	v_lshlrev_b32_e32 v153, 2, v86
	v_xor_b32_e32 v86, 32, v47
	v_writelane_b32 v254, s12, 18
	s_cmpk_gt_u32 s87, 0x1ff
	v_cmp_lt_i32_e32 vcc, v86, v85
	v_writelane_b32 v254, s13, 19
	s_cselect_b64 s[12:13], -1, 0
	s_add_i32 s10, 0, 0x22000
	v_cndmask_b32_e32 v47, v47, v86, vcc
	v_writelane_b32 v254, s12, 20
	v_lshl_add_u32 v155, v99, 2, s10
	v_xad_u32 v99, v92, -1, v91
	v_lshlrev_b32_e32 v154, 2, v47
	v_or_b32_e32 v47, s33, v140
	s_movk_i32 s1, 0x110
	v_or_b32_e32 v85, s2, v140
	v_or_b32_e32 v86, s3, v140
	v_or_b32_e32 v87, s4, v140
	v_or_b32_e32 v88, s5, v140
	v_or_b32_e32 v94, s6, v140
	v_or_b32_e32 v95, s7, v140
	v_or_b32_e32 v96, s9, v140
	v_or_b32_e32 v97, s11, v140
	v_or_b32_e32 v98, s0, v140
	v_writelane_b32 v254, s13, 21
	v_cmp_gt_u32_e64 s[12:13], s8, v99
	v_mul_lo_u32 v47, v47, s1
	v_mul_lo_u32 v85, v85, s1
	v_mul_lo_u32 v86, v86, s1
	v_mul_lo_u32 v87, v87, s1
	v_mul_lo_u32 v88, v88, s1
	v_mul_lo_u32 v94, v94, s1
	v_mul_lo_u32 v95, v95, s1
	v_mul_lo_u32 v96, v96, s1
	v_mul_lo_u32 v97, v97, s1
	v_mul_lo_u32 v98, v98, s1
	v_writelane_b32 v254, s12, 22
	s_movk_i32 s1, 0x7e
	v_lshl_add_u32 v156, v99, 2, s10
	v_writelane_b32 v254, s13, 23
	v_cmp_lt_u32_e64 s[12:13], s1, v92
	v_or_b32_e32 v99, 2, v92
	v_sub_u32_e32 v99, v91, v99
	v_writelane_b32 v254, s12, 24
	v_or_b32_e32 v92, 3, v92
	v_sub_u32_e32 v92, v91, v92
	v_writelane_b32 v254, s13, 25
	v_cmp_gt_u32_e64 s[12:13], s8, v99
	v_lshl_add_u32 v158, v92, 2, s10
	v_lshl_add_u32 v157, v99, 2, s10
	v_writelane_b32 v254, s12, 26
	s_cmpk_gt_u32 s87, 0x17f
	s_mov_b32 s20, s90
	v_writelane_b32 v254, s13, 27
	v_cmp_gt_u32_e64 s[12:13], s8, v92
	v_or_b32_e32 v92, s2, v136
	v_sub_u32_e32 v99, v91, v92
	v_writelane_b32 v254, s12, 28
	v_lshl_add_u32 v159, v99, 2, s10
	v_add_u32_e32 v197, s10, v93
	v_writelane_b32 v254, s13, 29
	v_cmp_gt_u32_e64 s[12:13], s8, v99
	v_xad_u32 v99, v92, -1, v91
	v_lshl_add_u32 v160, v99, 2, s10
	v_writelane_b32 v254, s12, 30
	v_lshlrev_b32_e32 v148, 2, v46
	v_lshlrev_b32_e32 v89, 5, v141
	v_writelane_b32 v254, s13, 31
	v_cmp_gt_u32_e64 s[12:13], s8, v99
	v_or_b32_e32 v99, 2, v92
	v_sub_u32_e32 v99, v91, v99
	v_writelane_b32 v254, s12, 32
	v_lshl_add_u32 v161, v99, 2, s10
	v_lshrrev_b32_e32 v46, 1, v0
	v_writelane_b32 v254, s13, 33
	v_cmp_lt_u32_e64 s[12:13], s1, v92
	v_or_b32_e32 v92, 3, v92
	v_sub_u32_e32 v92, v91, v92
	v_writelane_b32 v254, s12, 34
	v_lshl_add_u32 v162, v92, 2, s10
	v_and_b32_e32 v84, 24, v46
	v_writelane_b32 v254, s13, 35
	v_cmp_gt_u32_e64 s[12:13], s8, v99
	v_mov_b32_e32 v46, 0
	v_add_u32_e32 v89, 0, v89
	v_writelane_b32 v254, s12, 36
	s_mov_b32 s21, 0
	v_mov_b32_e32 v137, v46
	v_writelane_b32 v254, s13, 37
	v_cmp_gt_u32_e64 s[12:13], s8, v92
	v_or_b32_e32 v92, s3, v136
	v_sub_u32_e32 v99, v91, v92
	v_writelane_b32 v254, s12, 38
	v_cmp_gt_u32_e64 s[2:3], s8, v99
	v_lshl_add_u32 v163, v99, 2, s10
	v_writelane_b32 v254, s13, 39
	v_writelane_b32 v254, s2, 40
	v_xad_u32 v99, v92, -1, v91
	v_lshl_add_u32 v164, v99, 2, s10
	v_writelane_b32 v254, s3, 41
	s_cselect_b64 s[2:3], -1, 0
	v_writelane_b32 v254, s2, 42
	s_cmpk_gt_u32 s33, 0x4f
	v_mov_b32_e32 v198, 0x358637bd
	v_writelane_b32 v254, s3, 43
	v_cmp_gt_u32_e64 s[2:3], s8, v99
	v_or_b32_e32 v99, 2, v92
	v_sub_u32_e32 v99, v91, v99
	v_writelane_b32 v254, s2, 44
	v_lshl_add_u32 v165, v99, 2, s10
	s_mov_b32 s53, 0xf800000
	v_writelane_b32 v254, s3, 45
	v_cmp_lt_u32_e64 s[2:3], s1, v92
	v_or_b32_e32 v92, 3, v92
	v_sub_u32_e32 v92, v91, v92
	v_writelane_b32 v254, s2, 46
	v_lshl_add_u32 v166, v92, 2, s10
	v_mov_b32_e32 v199, 0x260
	v_writelane_b32 v254, s3, 47
	v_cmp_gt_u32_e64 s[2:3], s8, v99
	v_add_u32_e32 v200, 0x23200, v89
	s_movk_i32 s38, 0x4c00
	v_writelane_b32 v254, s2, 48
	s_movk_i32 s39, 0x1000
	s_movk_i32 s40, 0x3000
	v_writelane_b32 v254, s3, 49
	v_cmp_gt_u32_e64 s[2:3], s8, v92
	v_or_b32_e32 v92, s4, v136
	v_sub_u32_e32 v99, v91, v92
	v_writelane_b32 v254, s2, 50
	v_lshl_add_u32 v167, v99, 2, s10
	v_lshlrev_b32_e32 v138, 1, v84
	v_writelane_b32 v254, s3, 51
	v_cmp_gt_u32_e64 s[2:3], s8, v99
	v_xad_u32 v99, v92, -1, v91
	v_lshl_add_u32 v168, v99, 2, s10
	v_writelane_b32 v254, s2, 52
	v_add_u32_e32 v201, v90, v47
	v_add_u32_e32 v202, v90, v85
	v_writelane_b32 v254, s3, 53
	s_cselect_b64 s[2:3], -1, 0
	v_writelane_b32 v254, s2, 54
	s_cmpk_gt_u32 s87, 0xff
	s_cselect_b64 s[26:27], -1, 0
	v_writelane_b32 v254, s3, 55
	v_cmp_gt_u32_e64 s[2:3], s8, v99
	v_or_b32_e32 v99, 2, v92
	v_sub_u32_e32 v99, v91, v99
	v_writelane_b32 v254, s2, 56
	v_lshl_add_u32 v169, v99, 2, s10
	s_cmp_gt_u32 s33, 47
	v_writelane_b32 v254, s3, 57
	v_cmp_lt_u32_e64 s[2:3], s1, v92
	v_or_b32_e32 v92, 3, v92
	v_sub_u32_e32 v92, v91, v92
	v_writelane_b32 v254, s2, 58
	v_cmp_gt_u32_e64 s[12:13], s8, v92
	v_lshl_add_u32 v170, v92, 2, s10
	v_or_b32_e32 v92, s5, v136
	v_writelane_b32 v254, s3, 59
	v_cmp_gt_u32_e64 s[2:3], s8, v99
	v_sub_u32_e32 v99, v91, v92
	v_cmp_gt_u32_e64 s[14:15], s8, v99
	v_lshl_add_u32 v171, v99, 2, s10
	v_xad_u32 v99, v92, -1, v91
	v_cmp_gt_u32_e64 s[16:17], s8, v99
	v_cmp_lt_u32_e64 s[54:55], s1, v92
	v_lshl_add_u32 v172, v99, 2, s10
	v_or_b32_e32 v99, 2, v92
	v_or_b32_e32 v92, 3, v92
	v_sub_u32_e32 v92, v91, v92
	v_sub_u32_e32 v99, v91, v99
	v_cmp_gt_u32_e64 s[58:59], s8, v92
	v_lshl_add_u32 v174, v92, 2, s10
	v_or_b32_e32 v92, s6, v136
	v_cmp_gt_u32_e64 s[56:57], s8, v99
	v_lshl_add_u32 v173, v99, 2, s10
	v_sub_u32_e32 v99, v91, v92
	v_cmp_gt_u32_e64 s[60:61], s8, v99
	v_lshl_add_u32 v175, v99, 2, s10
	v_xad_u32 v99, v92, -1, v91
	v_cmp_gt_u32_e64 s[62:63], s8, v99
	v_cmp_lt_u32_e64 s[64:65], s1, v92
	v_lshl_add_u32 v176, v99, 2, s10
	v_or_b32_e32 v99, 2, v92
	v_or_b32_e32 v92, 3, v92
	v_sub_u32_e32 v92, v91, v92
	v_sub_u32_e32 v99, v91, v99
	v_cmp_gt_u32_e64 s[68:69], s8, v92
	v_lshl_add_u32 v178, v92, 2, s10
	v_or_b32_e32 v92, s7, v136
	v_cmp_gt_u32_e64 s[66:67], s8, v99
	v_lshl_add_u32 v177, v99, 2, s10
	v_sub_u32_e32 v99, v91, v92
	v_cmp_gt_u32_e64 s[70:71], s8, v99
	v_lshl_add_u32 v179, v99, 2, s10
	v_xad_u32 v99, v92, -1, v91
	v_cmp_gt_u32_e64 s[72:73], s8, v99
	v_cmp_lt_u32_e64 s[74:75], s1, v92
	v_lshl_add_u32 v180, v99, 2, s10
	v_or_b32_e32 v99, 2, v92
	v_or_b32_e32 v92, 3, v92
	v_sub_u32_e32 v92, v91, v92
	v_sub_u32_e32 v99, v91, v99
	v_cmp_gt_u32_e64 s[78:79], s8, v92
	v_lshl_add_u32 v182, v92, 2, s10
	v_or_b32_e32 v92, s9, v136
	v_cmp_gt_u32_e64 s[76:77], s8, v99
	v_lshl_add_u32 v181, v99, 2, s10
	v_sub_u32_e32 v99, v91, v92
	v_cmp_gt_u32_e64 s[80:81], s8, v99
	v_lshl_add_u32 v183, v99, 2, s10
	v_xad_u32 v99, v92, -1, v91
	v_cmp_gt_u32_e64 s[82:83], s8, v99
	v_cmp_lt_u32_e64 s[84:85], s1, v92
	v_lshl_add_u32 v184, v99, 2, s10
	v_or_b32_e32 v99, 2, v92
	v_or_b32_e32 v92, 3, v92
	v_writelane_b32 v254, s2, 60
	v_sub_u32_e32 v92, v91, v92
	v_sub_u32_e32 v99, v91, v99
	v_writelane_b32 v254, s3, 61
	v_cmp_gt_u32_e64 s[88:89], s8, v92
	v_lshl_add_u32 v186, v92, 2, s10
	v_or_b32_e32 v92, s11, v136
	s_cselect_b64 s[28:29], -1, 0
	v_writelane_b32 v254, s87, 62
	s_cmpk_gt_u32 s87, 0x7f
	v_cmp_gt_u32_e64 s[86:87], s8, v99
	v_lshl_add_u32 v185, v99, 2, s10
	v_sub_u32_e32 v99, v91, v92
	v_cmp_gt_u32_e64 s[90:91], s8, v99
	v_lshl_add_u32 v187, v99, 2, s10
	v_xad_u32 v99, v92, -1, v91
	v_cmp_gt_u32_e64 s[92:93], s8, v99
	v_lshl_add_u32 v188, v99, 2, s10
	v_or_b32_e32 v99, 2, v92
	v_or_b32_e32 v92, 3, v92
	v_sub_u32_e32 v92, v91, v92
	v_sub_u32_e32 v99, v91, v99
	v_cmp_gt_u32_e64 s[96:97], s8, v92
	v_lshl_add_u32 v190, v92, 2, s10
	v_or_b32_e32 v92, s0, v136
	v_cmp_gt_u32_e64 s[94:95], s8, v99
	v_lshl_add_u32 v189, v99, 2, s10
	v_sub_u32_e32 v99, v91, v92
	v_cmp_gt_u32_e64 s[0:1], s8, v99
	v_lshl_add_u32 v191, v99, 2, s10
	v_xad_u32 v99, v92, -1, v91
	s_cselect_b64 s[22:23], -1, 0
	v_cmp_gt_u32_e64 s[4:5], s8, v99
	v_lshl_add_u32 v192, v99, 2, s10
	v_or_b32_e32 v99, 2, v92
	v_or_b32_e32 v92, 3, v92
	s_add_u32 s30, s50, 0x22600000
	v_sub_u32_e32 v99, v91, v99
	v_sub_u32_e32 v91, v91, v92
	s_addc_u32 s31, s51, 0
	v_lshl_add_u32 v193, v99, 2, s10
	v_lshl_add_u32 v195, v91, 2, s10
	s_add_u32 s10, s50, 0x200000
	s_addc_u32 s11, s51, 0
	v_writelane_b32 v254, s10, 63
	v_cmp_gt_u32_e64 s[6:7], s8, v99
	v_cmp_gt_u32_e64 s[2:3], s8, v91
	v_writelane_b32 v255, s11, 0
	s_mov_b32 s10, s20
	v_writelane_b32 v255, s10, 1
	v_cmp_gt_u32_e64 s[8:9], s8, v0
	v_add_u32_e32 v203, v90, v86
	v_add_u32_e32 v204, v90, v87
	v_add_u32_e32 v205, v90, v88
	v_add_u32_e32 v206, v90, v94
	v_add_u32_e32 v207, v90, v95
	v_add_u32_e32 v208, v90, v96
	v_add_u32_e32 v209, v90, v97
	v_add_u32_e32 v210, v90, v98
	s_mov_b32 s41, 0xc3e00000
	v_mov_b32_e32 v211, 0x42000000
	v_mov_b32_e32 v212, 0x43e00000
	v_mov_b32_e32 v213, 0x41b17218
	v_writelane_b32 v255, s11, 2
	s_mov_b32 s42, s20
	s_branch .LBB0_707
